# code placement: the two post-barrier branch targets of each attention main loop aligned to 64-byte lines (pads in unreachable / rare-path spots); rest as v052
# baseline (speedup 1.0000x reference)
.LBB0_266:
	v_add_f32_e32 v2, v2, v4
	v_add_f32_e32 v2, v2, v5
	v_add_f32_e32 v2, v2, v6
	v_add_f32_e32 v2, v2, v7
	v_add_f32_e32 v2, v2, v8
	v_add_f32_e32 v2, v2, v9
	v_add_f32_e32 v2, v2, v10
	v_add_f32_e32 v2, v2, v11
	v_add_f32_e32 v2, v2, v12
	v_add_f32_e32 v2, v2, v13
	v_add_f32_e32 v2, v2, v14
	v_add_f32_e32 v2, v2, v15
	v_add_f32_e32 v2, v2, v16
	v_add_f32_e32 v2, v2, v17
	v_add_f32_e32 v2, v2, v18
	v_add_f32_e32 v2, v19, v2
	v_add_f32_e32 v2, v20, v2
	v_add_f32_e32 v2, v21, v2
	v_add_f32_e32 v2, v22, v2
	v_add_f32_e32 v2, v23, v2
	v_add_f32_e32 v2, v24, v2
	v_add_f32_e32 v2, v25, v2
	v_add_f32_e32 v2, v26, v2
	v_add_f32_e32 v2, v27, v2
	v_add_f32_e32 v2, v28, v2
	v_add_f32_e32 v2, v29, v2
	v_add_f32_e32 v2, v30, v2
	s_and_b32 s2, s2, 0x3fffffc0
	v_lshlrev_b32_e32 v35, 1, v36
	v_add_f32_e32 v2, v31, v2
	v_and_b32_e32 v237, 32, v35
	v_lshrrev_b32_e32 v35, 2, v36
	s_lshl_b32 s2, s2, 2
	v_add_f32_e32 v2, v32, v2
	v_and_or_b32 v35, v35, 3, v239
	s_add_i32 s39, s2, 0
	v_add_f32_e32 v2, v33, v2
	v_lshlrev_b32_e32 v236, 6, v35
	v_add_u32_e32 v35, 0, v237
	s_add_i32 s39, s39, 0x16000
	v_add_f32_e32 v2, v34, v2
	v_add3_u32 v242, v35, v233, v236
	v_add_f32_e32 v243, 0, v2
	s_mov_b32 s87, 1
	s_andn2_b64 vcc, exec, s[0:1]
	v_cmp_gt_u32_e64 s[2:3], 32, v230
	v_lshl_add_u32 v235, v231, 2, s39
	v_lshl_add_u32 v234, v239, 2, s39
	s_cbranch_vccnz .LBB0_281
	v_mov_b32_e32 v16, v3
	v_mov_b32_e32 v17, v3
	s_mov_b64 s[0:1], 0x168000
	v_mov_b32_e32 v2, v3
	v_mov_b32_e32 v4, v3
	v_mov_b32_e32 v5, v3
	v_mov_b32_e32 v6, v3
	v_mov_b32_e32 v7, v3
	v_mov_b32_e32 v8, v3
	v_mov_b32_e32 v9, v3
	v_mov_b32_e32 v10, v3
	v_mov_b32_e32 v11, v3
	v_mov_b32_e32 v12, v3
	v_mov_b32_e32 v13, v3
	v_mov_b32_e32 v14, v3
	v_mov_b32_e32 v15, v3
	v_mov_b64_e32 v[80:81], v[16:17]
	v_mov_b64_e32 v[64:65], v[16:17]
	v_mov_b64_e32 v[48:49], v[16:17]
	v_mov_b64_e32 v[32:33], v[16:17]
	s_add_i32 s42, s85, -7
	v_lshl_add_u64 v[206:207], v[216:217], 0, s[0:1]
	v_lshl_add_u64 v[208:209], v[220:221], 0, s[30:31]
	v_lshl_add_u64 v[210:211], v[218:219], 0, s[30:31]
	s_mov_b32 s86, 0xc000
	s_mov_b32 s33, 0
	s_movk_i32 s88, 0x4000
	s_movk_i32 s75, 0x2000
	v_mov_b64_e32 v[78:79], v[14:15]
	v_mov_b64_e32 v[76:77], v[12:13]
	v_mov_b64_e32 v[74:75], v[10:11]
	v_mov_b64_e32 v[72:73], v[8:9]
	v_mov_b64_e32 v[70:71], v[6:7]
	v_mov_b64_e32 v[68:69], v[4:5]
	v_mov_b64_e32 v[66:67], v[2:3]
	v_mov_b64_e32 v[62:63], v[14:15]
	v_mov_b64_e32 v[60:61], v[12:13]
	v_mov_b64_e32 v[58:59], v[10:11]
	v_mov_b64_e32 v[56:57], v[8:9]
	v_mov_b64_e32 v[54:55], v[6:7]
	v_mov_b64_e32 v[52:53], v[4:5]
	v_mov_b64_e32 v[50:51], v[2:3]
	v_mov_b64_e32 v[46:47], v[14:15]
	v_mov_b64_e32 v[44:45], v[12:13]
	v_mov_b64_e32 v[42:43], v[10:11]
	v_mov_b64_e32 v[40:41], v[8:9]
	v_mov_b64_e32 v[38:39], v[6:7]
	v_mov_b64_e32 v[36:37], v[4:5]
	v_mov_b64_e32 v[34:35], v[2:3]
	v_mov_b64_e32 v[30:31], v[14:15]
	v_mov_b64_e32 v[28:29], v[12:13]
	v_mov_b64_e32 v[26:27], v[10:11]
	v_mov_b64_e32 v[24:25], v[8:9]
	v_mov_b64_e32 v[22:23], v[6:7]
	v_mov_b64_e32 v[20:21], v[4:5]
	v_mov_b64_e32 v[18:19], v[2:3]
	v_mov_b32_e32 v82, v97
	v_mov_b32_e32 v83, v97
	v_mov_b32_e32 v84, v97
	v_mov_b32_e32 v85, v97
	v_mov_b32_e32 v86, v97
	v_mov_b32_e32 v87, v97
	v_mov_b32_e32 v88, v97
	v_mov_b32_e32 v89, v97
	v_mov_b32_e32 v90, v97
	v_mov_b32_e32 v91, v97
	v_mov_b32_e32 v92, v97
	v_mov_b32_e32 v93, v97
	v_mov_b32_e32 v94, v97
	v_mov_b32_e32 v95, v97
	v_mov_b32_e32 v96, v97
	s_branch .LBB0_269
	s_nop 0
	s_nop 0
	s_nop 0
	s_nop 0
	s_nop 0
	s_nop 0
	s_nop 0
	s_nop 0
	s_nop 0
	s_nop 0
	s_nop 0
	s_nop 0
	s_nop 0
	s_nop 0

.LBB0_270:
	s_waitcnt lgkmcnt(14)
	v_mfma_f32_32x32x16_bf16 v[66:81], v[138:141], v[202:205], v[66:81]
	v_exp_f32_e32 v114, v114
	v_exp_f32_e32 v115, v115
	v_exp_f32_e32 v116, v116
	v_exp_f32_e32 v117, v117
	ds_read_b64_tr_b16 v[166:167], v2 offset:32768
	ds_read_b64_tr_b16 v[168:169], v2 offset:33280
	s_waitcnt lgkmcnt(14)
	v_mfma_f32_32x32x16_bf16 v[50:65], v[138:141], v[198:201], v[50:65]
	v_exp_f32_e32 v118, v118
	v_exp_f32_e32 v119, v119
	v_exp_f32_e32 v120, v120
	v_exp_f32_e32 v121, v121
	ds_read_b64_tr_b16 v[174:175], v2 offset:36864
	ds_read_b64_tr_b16 v[176:177], v2 offset:37376
	s_waitcnt lgkmcnt(14)
	v_mfma_f32_32x32x16_bf16 v[66:81], v[134:137], v[194:197], v[66:81]
	v_exp_f32_e32 v122, v122
	v_exp_f32_e32 v123, v123
	v_exp_f32_e32 v124, v124
	v_exp_f32_e32 v125, v125
	ds_read_b64_tr_b16 v[178:179], v2 offset:33792
	ds_read_b64_tr_b16 v[180:181], v2 offset:34304
	s_waitcnt lgkmcnt(14)
	v_mfma_f32_32x32x16_bf16 v[50:65], v[134:137], v[170:173], v[50:65]
	v_exp_f32_e32 v126, v126
	v_exp_f32_e32 v127, v127
	v_exp_f32_e32 v128, v128
	v_exp_f32_e32 v129, v129
	ds_read_b64_tr_b16 v[182:183], v2 offset:37888
	ds_read_b64_tr_b16 v[184:185], v2 offset:38400
	s_waitcnt lgkmcnt(14)
	v_mfma_f32_32x32x16_bf16 v[66:81], v[130:133], v[162:165], v[66:81]
	v_exp_f32_e32 v98, v98
	v_exp_f32_e32 v99, v99
	v_exp_f32_e32 v100, v100
	v_exp_f32_e32 v101, v101
	ds_read_b64_tr_b16 v[186:187], v2 offset:34816
	ds_read_b64_tr_b16 v[188:189], v2 offset:35328
	s_waitcnt lgkmcnt(14)
	v_mfma_f32_32x32x16_bf16 v[50:65], v[130:133], v[12:15], v[50:65]
	v_exp_f32_e32 v102, v102
	v_exp_f32_e32 v103, v103
	v_exp_f32_e32 v104, v104
	v_exp_f32_e32 v105, v105
	ds_read_b64_tr_b16 v[190:191], v2 offset:38912
	ds_read_b64_tr_b16 v[192:193], v2 offset:39424
	s_waitcnt lgkmcnt(14)
	v_mfma_f32_32x32x16_bf16 v[66:81], v[158:161], v[8:11], v[66:81]
	v_exp_f32_e32 v106, v106
	v_exp_f32_e32 v107, v107
	v_exp_f32_e32 v108, v108
	v_exp_f32_e32 v109, v109
	ds_read_b64_tr_b16 v[194:195], v2 offset:35840
	ds_read_b64_tr_b16 v[196:197], v2 offset:36352
	s_waitcnt lgkmcnt(14)
	v_mfma_f32_32x32x16_bf16 v[50:65], v[158:161], v[4:7], v[50:65]
	v_exp_f32_e32 v110, v110
	v_exp_f32_e32 v111, v111
	v_exp_f32_e32 v112, v112
	v_exp_f32_e32 v113, v113
	ds_read_b64_tr_b16 v[4:5], v2 offset:39936
	ds_read_b64_tr_b16 v[6:7], v2 offset:40448
	v_add_f32_e32 v2, v114, v115
	s_waitcnt lgkmcnt(14)
	v_mfma_f32_32x32x16_bf16 v[34:49], v[138:141], v[166:169], v[34:49]
	v_add_f32_e32 v2, v116, v2
	v_add_f32_e32 v2, v117, v2
	v_add_f32_e32 v2, v118, v2
	v_add_f32_e32 v2, v119, v2
	v_add_u32_e32 v16, s88, v240
	ds_read_b128 v[12:15], v16
	ds_read_b128 v[8:11], v16 offset:512
	s_waitcnt lgkmcnt(14)
	v_mfma_f32_32x32x16_bf16 v[18:33], v[138:141], v[174:177], v[18:33]
	v_add_f32_e32 v2, v120, v2
	v_add_f32_e32 v2, v121, v2
	v_add_f32_e32 v2, v122, v2
	v_add_f32_e32 v2, v123, v2
	ds_read_b128 v[166:169], v16 offset:2048
	ds_read_b128 v[162:165], v16 offset:2560
	s_waitcnt lgkmcnt(14)
	v_mfma_f32_32x32x16_bf16 v[34:49], v[134:137], v[178:181], v[34:49]
	v_add_f32_e32 v2, v124, v2
	v_add_f32_e32 v2, v125, v2
	v_add_f32_e32 v2, v126, v2
	v_add_f32_e32 v2, v127, v2
	v_cvt_pk_bf16_f32 v138, v114, v115
	v_cvt_pk_bf16_f32 v139, v116, v117
	ds_read_b128 v[174:177], v16 offset:4096
	ds_read_b128 v[170:173], v16 offset:4608
	s_waitcnt lgkmcnt(14)
	v_mfma_f32_32x32x16_bf16 v[18:33], v[134:137], v[182:185], v[18:33]
	v_add_f32_e32 v2, v128, v2
	v_add_f32_e32 v2, v129, v2
	v_add_f32_e32 v2, v98, v2
	v_add_f32_e32 v2, v99, v2
	v_cvt_pk_bf16_f32 v140, v118, v119
	v_cvt_pk_bf16_f32 v141, v120, v121
	ds_read_b128 v[182:185], v16 offset:6144
	ds_read_b128 v[178:181], v16 offset:6656
	s_waitcnt lgkmcnt(14)
	v_mfma_f32_32x32x16_bf16 v[34:49], v[130:133], v[186:189], v[34:49]
	v_add_f32_e32 v2, v100, v2
	v_add_f32_e32 v2, v101, v2
	v_add_f32_e32 v2, v102, v2
	v_add_f32_e32 v2, v103, v2
	v_cvt_pk_bf16_f32 v134, v122, v123
	v_cvt_pk_bf16_f32 v135, v124, v125
	s_waitcnt lgkmcnt(12)
	v_mfma_f32_32x32x16_bf16 v[18:33], v[130:133], v[190:193], v[18:33]
	v_add_f32_e32 v2, v104, v2
	v_add_f32_e32 v2, v105, v2
	v_add_f32_e32 v2, v106, v2
	v_add_f32_e32 v2, v107, v2
	v_cvt_pk_bf16_f32 v136, v126, v127
	v_cvt_pk_bf16_f32 v137, v128, v129
	s_waitcnt lgkmcnt(10)
	v_mfma_f32_32x32x16_bf16 v[34:49], v[158:161], v[194:197], v[34:49]
	v_add_f32_e32 v2, v108, v2
	v_add_f32_e32 v2, v109, v2
	v_add_f32_e32 v2, v110, v2
	v_add_f32_e32 v2, v111, v2
	v_cvt_pk_bf16_f32 v130, v98, v99
	v_cvt_pk_bf16_f32 v131, v100, v101
	s_waitcnt lgkmcnt(8)
	v_mfma_f32_32x32x16_bf16 v[18:33], v[158:161], v[4:7], v[18:33]
	v_add_f32_e32 v2, v112, v2
	v_add_f32_e32 v2, v113, v2
	v_cvt_pk_bf16_f32 v132, v102, v103
	v_cvt_pk_bf16_f32 v133, v104, v105
	v_cvt_pk_bf16_f32 v4, v106, v107
	v_cvt_pk_bf16_f32 v5, v108, v109
	v_cvt_pk_bf16_f32 v6, v110, v111
	v_cvt_pk_bf16_f32 v7, v112, v113
	s_waitcnt vmcnt(3) lgkmcnt(0)
	s_barrier
	s_andn2_b64 vcc, exec, s[0:1]
	s_cbranch_vccnz .LBB0_272
	s_waitcnt lgkmcnt(0)
	ds_read2_b32 v[16:17], v234 offset1:1
	ds_read2_b32 v[98:99], v234 offset0:2 offset1:3
	ds_read2_b32 v[100:101], v234 offset0:8 offset1:9
	ds_read2_b32 v[102:103], v234 offset0:10 offset1:11
	s_waitcnt lgkmcnt(3)
	v_mul_f32_e32 v66, v66, v16
	v_mul_f32_e32 v50, v50, v16
	v_mul_f32_e32 v34, v34, v16
	v_mul_f32_e32 v18, v18, v16
	v_mul_f32_e32 v67, v67, v17
	v_mul_f32_e32 v51, v51, v17
	v_mul_f32_e32 v35, v35, v17
	v_mul_f32_e32 v19, v19, v17
	s_waitcnt lgkmcnt(2)
	v_mul_f32_e32 v68, v68, v98
	v_mul_f32_e32 v52, v52, v98
	v_mul_f32_e32 v36, v36, v98
	v_mul_f32_e32 v20, v20, v98
	v_mul_f32_e32 v69, v69, v99
	v_mul_f32_e32 v53, v53, v99
	v_mul_f32_e32 v37, v37, v99
	v_mul_f32_e32 v21, v21, v99
	s_waitcnt lgkmcnt(1)
	v_mul_f32_e32 v70, v70, v100
	v_mul_f32_e32 v54, v54, v100
	v_mul_f32_e32 v38, v38, v100
	v_mul_f32_e32 v22, v22, v100
	v_mul_f32_e32 v71, v71, v101
	v_mul_f32_e32 v55, v55, v101
	v_mul_f32_e32 v39, v39, v101
	v_mul_f32_e32 v23, v23, v101
	s_waitcnt lgkmcnt(0)
	v_mul_f32_e32 v72, v72, v102
	v_mul_f32_e32 v56, v56, v102
	v_mul_f32_e32 v40, v40, v102
	v_mul_f32_e32 v24, v24, v102
	v_mul_f32_e32 v73, v73, v103
	v_mul_f32_e32 v57, v57, v103
	v_mul_f32_e32 v41, v41, v103
	ds_read2_b32 v[16:17], v234 offset0:16 offset1:17
	v_mul_f32_e32 v25, v25, v103
	ds_read2_b32 v[98:99], v234 offset0:18 offset1:19
	ds_read2_b32 v[100:101], v234 offset0:24 offset1:25
	ds_read2_b32 v[102:103], v234 offset0:26 offset1:27
	s_waitcnt lgkmcnt(3)
	v_mul_f32_e32 v74, v74, v16
	v_mul_f32_e32 v58, v58, v16
	v_mul_f32_e32 v42, v42, v16
	v_mul_f32_e32 v26, v26, v16
	v_mul_f32_e32 v75, v75, v17
	v_mul_f32_e32 v59, v59, v17
	v_mul_f32_e32 v43, v43, v17
	v_mul_f32_e32 v27, v27, v17
	s_waitcnt lgkmcnt(2)
	v_mul_f32_e32 v76, v76, v98
	v_mul_f32_e32 v60, v60, v98
	v_mul_f32_e32 v44, v44, v98
	v_mul_f32_e32 v28, v28, v98
	v_mul_f32_e32 v77, v77, v99
	v_mul_f32_e32 v61, v61, v99
	v_mul_f32_e32 v45, v45, v99
	v_mul_f32_e32 v29, v29, v99
	s_waitcnt lgkmcnt(1)
	v_mul_f32_e32 v78, v78, v100
	v_mul_f32_e32 v62, v62, v100
	v_mul_f32_e32 v46, v46, v100
	v_mul_f32_e32 v30, v30, v100
	v_mul_f32_e32 v79, v79, v101
	v_mul_f32_e32 v63, v63, v101
	v_mul_f32_e32 v47, v47, v101
	v_mul_f32_e32 v31, v31, v101
	s_waitcnt lgkmcnt(0)
	v_mul_f32_e32 v80, v80, v102
	v_mul_f32_e32 v64, v64, v102
	v_mul_f32_e32 v48, v48, v102
	v_mul_f32_e32 v32, v32, v102
	v_mul_f32_e32 v81, v81, v103
	v_mul_f32_e32 v65, v65, v103
	v_mul_f32_e32 v49, v49, v103
	v_mul_f32_e32 v33, v33, v103
	s_nop 0
	s_nop 0
	s_nop 0
	s_nop 0
	s_nop 0
	s_nop 0
	s_nop 0
	s_nop 0
	s_nop 0
	s_nop 0
	s_nop 0
	s_nop 0
	s_nop 0

.LBB0_346:
	v_max_f32_e32 v16, v16, v16
	v_max_f32_e32 v17, 0, v16
	v_exp_f32_e64 v16, -v17
	v_cmp_gt_u32_e32 vcc, 32, v230
	s_and_saveexec_b64 s[2:3], vcc
	ds_write_b32 v235, v16
	s_or_b64 exec, exec, s[2:3]
	v_sub_f32_e32 v113, v113, v17
	v_sub_f32_e32 v112, v112, v17
	v_sub_f32_e32 v111, v111, v17
	v_sub_f32_e32 v110, v110, v17
	v_sub_f32_e32 v109, v109, v17
	v_sub_f32_e32 v108, v108, v17
	v_sub_f32_e32 v107, v107, v17
	v_sub_f32_e32 v106, v106, v17
	v_sub_f32_e32 v105, v105, v17
	v_sub_f32_e32 v104, v104, v17
	v_sub_f32_e32 v103, v103, v17
	v_sub_f32_e32 v102, v102, v17
	v_sub_f32_e32 v101, v101, v17
	v_sub_f32_e32 v100, v100, v17
	v_sub_f32_e32 v99, v99, v17
	v_sub_f32_e32 v98, v98, v17
	v_sub_f32_e32 v97, v97, v17
	v_sub_f32_e32 v96, v96, v17
	v_sub_f32_e32 v95, v95, v17
	v_sub_f32_e32 v94, v94, v17
	v_sub_f32_e32 v93, v93, v17
	v_sub_f32_e32 v92, v92, v17
	v_sub_f32_e32 v91, v91, v17
	v_sub_f32_e32 v90, v90, v17
	v_sub_f32_e32 v89, v89, v17
	v_sub_f32_e32 v88, v88, v17
	v_sub_f32_e32 v87, v87, v17
	v_sub_f32_e32 v86, v86, v17
	v_sub_f32_e32 v85, v85, v17
	v_sub_f32_e32 v84, v84, v17
	v_sub_f32_e32 v83, v83, v17
	v_sub_f32_e32 v82, v82, v17
	v_mul_f32_e32 v243, v243, v16
	s_branch .LBB0_340
	s_nop 0
	s_nop 0
	s_nop 0
	s_nop 0
	s_nop 0
.LBB0_349:
	v_mov_b32_e32 v52, v0
	s_barrier
	s_ashr_i32 s21, s20, 31
	v_readfirstlane_b32 s0, v52
	s_ashr_i32 s2, s0, 2
	s_and_b32 s36, s2, -16
	s_ashr_i32 s3, s0, 7
	v_lshlrev_b32_e32 v2, 4, v52
	v_and_b32_e32 v38, 48, v52
	v_mov_b32_e32 v39, 0
	v_and_b32_e32 v59, 48, v2
	v_lshl_add_u64 v[2:3], s[22:23], 0, v[38:39]
	s_mov_b64 s[0:1], 0x100000
	s_cmp_gt_i32 s3, -1
	v_lshl_add_u64 v[42:43], v[2:3], 0, s[0:1]
	s_cselect_b64 s[0:1], -1, 0
	s_cmp_gt_i32 s3, 0
	v_ashrrev_i32_e32 v58, 2, v52
	s_cselect_b64 s[24:25], -1, 0
	s_cmp_gt_i32 s3, 1
	s_movk_i32 s4, 0x1200
	v_and_b32_e32 v1, 63, v52
	s_cselect_b64 s[26:27], -1, 0
	s_cmp_gt_i32 s3, 2
	v_bfi_b32 v44, -16, s2, v52
	v_mad_i64_i32 v[2:3], s[2:3], v58, s4, 0
	v_mov_b32_e32 v8, 0x90000
	v_lshlrev_b32_e32 v1, 2, v1
	v_mad_i64_i32 v[2:3], s[2:3], s20, v8, v[2:3]
	v_xor_b32_e32 v45, 4, v1
	v_xor_b32_e32 v53, 8, v1
	s_cselect_b64 s[28:29], -1, 0
	v_and_b32_e32 v1, 3, v52
	s_add_u32 s2, s94, s41
	v_lshl_or_b32 v2, v1, 5, v2
	s_addc_u32 s3, s95, 0
	v_bfe_u32 v41, v52, 4, 2
	v_lshl_add_u64 v[46:47], s[2:3], 0, v[2:3]
	v_mad_i64_i32 v[2:3], s[4:5], v44, s4, 0
	v_lshlrev_b32_e32 v40, 3, v41
	v_mad_i64_i32 v[2:3], s[4:5], s20, v8, v[2:3]
	v_or_b32_e32 v2, v2, v40
	v_and_b32_e32 v55, 15, v52
	v_lshl_add_u64 v[2:3], s[2:3], 0, v[2:3]
	s_mov_b64 s[2:3], 0x10a00040
	v_lshl_add_u32 v4, v58, 1, 0
	v_add_u32_e32 v5, 0, v38
	v_mul_u32_u24_e32 v6, 0x110, v59
	v_mul_u32_u24_e32 v7, 0x110, v55
	v_lshl_add_u64 v[48:49], v[2:3], 0, s[2:3]
	v_cndmask_b32_e64 v2, 0, 1, s[0:1]
	s_mov_b64 s[30:31], 0
	s_mov_b64 s[34:35], 0x10a00200
	v_mov_b32_e32 v39, 0x3727c5ac
	s_mov_b32 s33, 0xf800000
	v_mov_b32_e32 v54, 0x260
	s_movk_i32 s37, 0x7fff
	v_add_u32_e32 v56, v4, v6
	v_cmp_ne_u32_e64 s[2:3], 1, v2
	v_add_u32_e32 v57, v5, v7
	v_mov_b32_e32 v60, 1
	v_readlane_b32 s41, v254, 39
	s_branch .LBB0_351

.LBB0_879:
	v_add_f32_e32 v2, v2, v4
	v_add_f32_e32 v2, v2, v5
	v_add_f32_e32 v2, v2, v6
	v_add_f32_e32 v2, v2, v7
	v_add_f32_e32 v2, v2, v8
	v_add_f32_e32 v2, v2, v9
	v_add_f32_e32 v2, v2, v10
	v_add_f32_e32 v2, v2, v11
	v_add_f32_e32 v2, v2, v12
	v_add_f32_e32 v2, v2, v13
	v_add_f32_e32 v2, v2, v14
	v_add_f32_e32 v2, v2, v15
	v_add_f32_e32 v2, v2, v16
	v_add_f32_e32 v2, v2, v17
	v_add_f32_e32 v2, v2, v18
	v_add_f32_e32 v2, v19, v2
	v_add_f32_e32 v2, v20, v2
	v_add_f32_e32 v2, v21, v2
	v_add_f32_e32 v2, v22, v2
	v_add_f32_e32 v2, v23, v2
	v_add_f32_e32 v2, v24, v2
	v_add_f32_e32 v2, v25, v2
	v_add_f32_e32 v2, v26, v2
	v_add_f32_e32 v2, v27, v2
	v_add_f32_e32 v2, v28, v2
	v_add_f32_e32 v2, v29, v2
	v_add_f32_e32 v2, v30, v2
	s_and_b32 s2, s2, 0x3fffffc0
	v_lshlrev_b32_e32 v35, 1, v36
	v_add_f32_e32 v2, v31, v2
	v_and_b32_e32 v237, 32, v35
	v_lshrrev_b32_e32 v35, 2, v36
	s_lshl_b32 s2, s2, 2
	v_add_f32_e32 v2, v32, v2
	v_and_or_b32 v35, v35, 3, v239
	s_add_i32 s31, s2, 0
	v_add_f32_e32 v2, v33, v2
	v_lshlrev_b32_e32 v236, 6, v35
	v_add_u32_e32 v35, 0, v237
	s_add_i32 s31, s31, 0x16000
	v_add_f32_e32 v2, v34, v2
	v_add3_u32 v242, v35, v233, v236
	v_add_f32_e32 v243, 0, v2
	s_mov_b32 s81, 1
	s_andn2_b64 vcc, exec, s[0:1]
	v_cmp_gt_u32_e64 s[2:3], 32, v230
	v_lshl_add_u32 v235, v231, 2, s31
	v_lshl_add_u32 v234, v239, 2, s31
	s_cbranch_vccnz .LBB0_894
	v_mov_b32_e32 v16, v3
	v_mov_b32_e32 v17, v3
	s_mov_b64 s[0:1], 0x168000
	v_mov_b32_e32 v2, v3
	v_mov_b32_e32 v4, v3
	v_mov_b32_e32 v5, v3
	v_mov_b32_e32 v6, v3
	v_mov_b32_e32 v7, v3
	v_mov_b32_e32 v8, v3
	v_mov_b32_e32 v9, v3
	v_mov_b32_e32 v10, v3
	v_mov_b32_e32 v11, v3
	v_mov_b32_e32 v12, v3
	v_mov_b32_e32 v13, v3
	v_mov_b32_e32 v14, v3
	v_mov_b32_e32 v15, v3
	v_mov_b64_e32 v[80:81], v[16:17]
	v_mov_b64_e32 v[64:65], v[16:17]
	v_mov_b64_e32 v[48:49], v[16:17]
	v_mov_b64_e32 v[32:33], v[16:17]
	s_add_i32 s34, s79, -7
	v_lshl_add_u64 v[206:207], v[216:217], 0, s[0:1]
	v_lshl_add_u64 v[208:209], v[220:221], 0, s[24:25]
	v_lshl_add_u64 v[210:211], v[218:219], 0, s[24:25]
	s_mov_b32 s80, 0xc000
	s_mov_b32 s43, 0
	s_movk_i32 s82, 0x4000
	s_movk_i32 s38, 0x2000
	v_mov_b64_e32 v[78:79], v[14:15]
	v_mov_b64_e32 v[76:77], v[12:13]
	v_mov_b64_e32 v[74:75], v[10:11]
	v_mov_b64_e32 v[72:73], v[8:9]
	v_mov_b64_e32 v[70:71], v[6:7]
	v_mov_b64_e32 v[68:69], v[4:5]
	v_mov_b64_e32 v[66:67], v[2:3]
	v_mov_b64_e32 v[62:63], v[14:15]
	v_mov_b64_e32 v[60:61], v[12:13]
	v_mov_b64_e32 v[58:59], v[10:11]
	v_mov_b64_e32 v[56:57], v[8:9]
	v_mov_b64_e32 v[54:55], v[6:7]
	v_mov_b64_e32 v[52:53], v[4:5]
	v_mov_b64_e32 v[50:51], v[2:3]
	v_mov_b64_e32 v[46:47], v[14:15]
	v_mov_b64_e32 v[44:45], v[12:13]
	v_mov_b64_e32 v[42:43], v[10:11]
	v_mov_b64_e32 v[40:41], v[8:9]
	v_mov_b64_e32 v[38:39], v[6:7]
	v_mov_b64_e32 v[36:37], v[4:5]
	v_mov_b64_e32 v[34:35], v[2:3]
	v_mov_b64_e32 v[30:31], v[14:15]
	v_mov_b64_e32 v[28:29], v[12:13]
	v_mov_b64_e32 v[26:27], v[10:11]
	v_mov_b64_e32 v[24:25], v[8:9]
	v_mov_b64_e32 v[22:23], v[6:7]
	v_mov_b64_e32 v[20:21], v[4:5]
	v_mov_b64_e32 v[18:19], v[2:3]
	v_mov_b32_e32 v82, v97
	v_mov_b32_e32 v83, v97
	v_mov_b32_e32 v84, v97
	v_mov_b32_e32 v85, v97
	v_mov_b32_e32 v86, v97
	v_mov_b32_e32 v87, v97
	v_mov_b32_e32 v88, v97
	v_mov_b32_e32 v89, v97
	v_mov_b32_e32 v90, v97
	v_mov_b32_e32 v91, v97
	v_mov_b32_e32 v92, v97
	v_mov_b32_e32 v93, v97
	v_mov_b32_e32 v94, v97
	v_mov_b32_e32 v95, v97
	v_mov_b32_e32 v96, v97
	s_branch .LBB0_882
	s_nop 0
	s_nop 0
	s_nop 0
	s_nop 0
	s_nop 0
	s_nop 0
	s_nop 0
	s_nop 0
	s_nop 0
	s_nop 0
	s_nop 0
	s_nop 0

.LBB0_883:
	s_waitcnt lgkmcnt(14)
	v_mfma_f32_32x32x16_bf16 v[66:81], v[138:141], v[202:205], v[66:81]
	v_exp_f32_e32 v114, v114
	v_exp_f32_e32 v115, v115
	v_exp_f32_e32 v116, v116
	v_exp_f32_e32 v117, v117
	ds_read_b64_tr_b16 v[166:167], v2 offset:32768
	ds_read_b64_tr_b16 v[168:169], v2 offset:33280
	s_waitcnt lgkmcnt(14)
	v_mfma_f32_32x32x16_bf16 v[50:65], v[138:141], v[198:201], v[50:65]
	v_exp_f32_e32 v118, v118
	v_exp_f32_e32 v119, v119
	v_exp_f32_e32 v120, v120
	v_exp_f32_e32 v121, v121
	ds_read_b64_tr_b16 v[174:175], v2 offset:36864
	ds_read_b64_tr_b16 v[176:177], v2 offset:37376
	s_waitcnt lgkmcnt(14)
	v_mfma_f32_32x32x16_bf16 v[66:81], v[134:137], v[194:197], v[66:81]
	v_exp_f32_e32 v122, v122
	v_exp_f32_e32 v123, v123
	v_exp_f32_e32 v124, v124
	v_exp_f32_e32 v125, v125
	ds_read_b64_tr_b16 v[178:179], v2 offset:33792
	ds_read_b64_tr_b16 v[180:181], v2 offset:34304
	s_waitcnt lgkmcnt(14)
	v_mfma_f32_32x32x16_bf16 v[50:65], v[134:137], v[170:173], v[50:65]
	v_exp_f32_e32 v126, v126
	v_exp_f32_e32 v127, v127
	v_exp_f32_e32 v128, v128
	v_exp_f32_e32 v129, v129
	ds_read_b64_tr_b16 v[182:183], v2 offset:37888
	ds_read_b64_tr_b16 v[184:185], v2 offset:38400
	s_waitcnt lgkmcnt(14)
	v_mfma_f32_32x32x16_bf16 v[66:81], v[130:133], v[162:165], v[66:81]
	v_exp_f32_e32 v98, v98
	v_exp_f32_e32 v99, v99
	v_exp_f32_e32 v100, v100
	v_exp_f32_e32 v101, v101
	ds_read_b64_tr_b16 v[186:187], v2 offset:34816
	ds_read_b64_tr_b16 v[188:189], v2 offset:35328
	s_waitcnt lgkmcnt(14)
	v_mfma_f32_32x32x16_bf16 v[50:65], v[130:133], v[12:15], v[50:65]
	v_exp_f32_e32 v102, v102
	v_exp_f32_e32 v103, v103
	v_exp_f32_e32 v104, v104
	v_exp_f32_e32 v105, v105
	ds_read_b64_tr_b16 v[190:191], v2 offset:38912
	ds_read_b64_tr_b16 v[192:193], v2 offset:39424
	s_waitcnt lgkmcnt(14)
	v_mfma_f32_32x32x16_bf16 v[66:81], v[158:161], v[8:11], v[66:81]
	v_exp_f32_e32 v106, v106
	v_exp_f32_e32 v107, v107
	v_exp_f32_e32 v108, v108
	v_exp_f32_e32 v109, v109
	ds_read_b64_tr_b16 v[194:195], v2 offset:35840
	ds_read_b64_tr_b16 v[196:197], v2 offset:36352
	s_waitcnt lgkmcnt(14)
	v_mfma_f32_32x32x16_bf16 v[50:65], v[158:161], v[4:7], v[50:65]
	v_exp_f32_e32 v110, v110
	v_exp_f32_e32 v111, v111
	v_exp_f32_e32 v112, v112
	v_exp_f32_e32 v113, v113
	ds_read_b64_tr_b16 v[4:5], v2 offset:39936
	ds_read_b64_tr_b16 v[6:7], v2 offset:40448
	v_add_f32_e32 v2, v114, v115
	s_waitcnt lgkmcnt(14)
	v_mfma_f32_32x32x16_bf16 v[34:49], v[138:141], v[166:169], v[34:49]
	v_add_f32_e32 v2, v116, v2
	v_add_f32_e32 v2, v117, v2
	v_add_f32_e32 v2, v118, v2
	v_add_f32_e32 v2, v119, v2
	v_add_u32_e32 v16, s82, v240
	ds_read_b128 v[12:15], v16
	ds_read_b128 v[8:11], v16 offset:512
	s_waitcnt lgkmcnt(14)
	v_mfma_f32_32x32x16_bf16 v[18:33], v[138:141], v[174:177], v[18:33]
	v_add_f32_e32 v2, v120, v2
	v_add_f32_e32 v2, v121, v2
	v_add_f32_e32 v2, v122, v2
	v_add_f32_e32 v2, v123, v2
	ds_read_b128 v[166:169], v16 offset:2048
	ds_read_b128 v[162:165], v16 offset:2560
	s_waitcnt lgkmcnt(14)
	v_mfma_f32_32x32x16_bf16 v[34:49], v[134:137], v[178:181], v[34:49]
	v_add_f32_e32 v2, v124, v2
	v_add_f32_e32 v2, v125, v2
	v_add_f32_e32 v2, v126, v2
	v_add_f32_e32 v2, v127, v2
	v_cvt_pk_bf16_f32 v138, v114, v115
	v_cvt_pk_bf16_f32 v139, v116, v117
	ds_read_b128 v[174:177], v16 offset:4096
	ds_read_b128 v[170:173], v16 offset:4608
	s_waitcnt lgkmcnt(14)
	v_mfma_f32_32x32x16_bf16 v[18:33], v[134:137], v[182:185], v[18:33]
	v_add_f32_e32 v2, v128, v2
	v_add_f32_e32 v2, v129, v2
	v_add_f32_e32 v2, v98, v2
	v_add_f32_e32 v2, v99, v2
	v_cvt_pk_bf16_f32 v140, v118, v119
	v_cvt_pk_bf16_f32 v141, v120, v121
	ds_read_b128 v[182:185], v16 offset:6144
	ds_read_b128 v[178:181], v16 offset:6656
	s_waitcnt lgkmcnt(14)
	v_mfma_f32_32x32x16_bf16 v[34:49], v[130:133], v[186:189], v[34:49]
	v_add_f32_e32 v2, v100, v2
	v_add_f32_e32 v2, v101, v2
	v_add_f32_e32 v2, v102, v2
	v_add_f32_e32 v2, v103, v2
	v_cvt_pk_bf16_f32 v134, v122, v123
	v_cvt_pk_bf16_f32 v135, v124, v125
	s_waitcnt lgkmcnt(12)
	v_mfma_f32_32x32x16_bf16 v[18:33], v[130:133], v[190:193], v[18:33]
	v_add_f32_e32 v2, v104, v2
	v_add_f32_e32 v2, v105, v2
	v_add_f32_e32 v2, v106, v2
	v_add_f32_e32 v2, v107, v2
	v_cvt_pk_bf16_f32 v136, v126, v127
	v_cvt_pk_bf16_f32 v137, v128, v129
	s_waitcnt lgkmcnt(10)
	v_mfma_f32_32x32x16_bf16 v[34:49], v[158:161], v[194:197], v[34:49]
	v_add_f32_e32 v2, v108, v2
	v_add_f32_e32 v2, v109, v2
	v_add_f32_e32 v2, v110, v2
	v_add_f32_e32 v2, v111, v2
	v_cvt_pk_bf16_f32 v130, v98, v99
	v_cvt_pk_bf16_f32 v131, v100, v101
	s_waitcnt lgkmcnt(8)
	v_mfma_f32_32x32x16_bf16 v[18:33], v[158:161], v[4:7], v[18:33]
	v_add_f32_e32 v2, v112, v2
	v_add_f32_e32 v2, v113, v2
	v_cvt_pk_bf16_f32 v132, v102, v103
	v_cvt_pk_bf16_f32 v133, v104, v105
	v_cvt_pk_bf16_f32 v4, v106, v107
	v_cvt_pk_bf16_f32 v5, v108, v109
	v_cvt_pk_bf16_f32 v6, v110, v111
	v_cvt_pk_bf16_f32 v7, v112, v113
	s_waitcnt vmcnt(3) lgkmcnt(0)
	s_barrier
	s_andn2_b64 vcc, exec, s[0:1]
	s_cbranch_vccnz .LBB0_885
	s_waitcnt lgkmcnt(0)
	ds_read2_b32 v[16:17], v234 offset1:1
	ds_read2_b32 v[98:99], v234 offset0:2 offset1:3
	ds_read2_b32 v[100:101], v234 offset0:8 offset1:9
	ds_read2_b32 v[102:103], v234 offset0:10 offset1:11
	s_waitcnt lgkmcnt(3)
	v_mul_f32_e32 v66, v66, v16
	v_mul_f32_e32 v50, v50, v16
	v_mul_f32_e32 v34, v34, v16
	v_mul_f32_e32 v18, v18, v16
	v_mul_f32_e32 v67, v67, v17
	v_mul_f32_e32 v51, v51, v17
	v_mul_f32_e32 v35, v35, v17
	v_mul_f32_e32 v19, v19, v17
	s_waitcnt lgkmcnt(2)
	v_mul_f32_e32 v68, v68, v98
	v_mul_f32_e32 v52, v52, v98
	v_mul_f32_e32 v36, v36, v98
	v_mul_f32_e32 v20, v20, v98
	v_mul_f32_e32 v69, v69, v99
	v_mul_f32_e32 v53, v53, v99
	v_mul_f32_e32 v37, v37, v99
	v_mul_f32_e32 v21, v21, v99
	s_waitcnt lgkmcnt(1)
	v_mul_f32_e32 v70, v70, v100
	v_mul_f32_e32 v54, v54, v100
	v_mul_f32_e32 v38, v38, v100
	v_mul_f32_e32 v22, v22, v100
	v_mul_f32_e32 v71, v71, v101
	v_mul_f32_e32 v55, v55, v101
	v_mul_f32_e32 v39, v39, v101
	v_mul_f32_e32 v23, v23, v101
	s_waitcnt lgkmcnt(0)
	v_mul_f32_e32 v72, v72, v102
	v_mul_f32_e32 v56, v56, v102
	v_mul_f32_e32 v40, v40, v102
	v_mul_f32_e32 v24, v24, v102
	v_mul_f32_e32 v73, v73, v103
	v_mul_f32_e32 v57, v57, v103
	v_mul_f32_e32 v41, v41, v103
	ds_read2_b32 v[16:17], v234 offset0:16 offset1:17
	v_mul_f32_e32 v25, v25, v103
	ds_read2_b32 v[98:99], v234 offset0:18 offset1:19
	ds_read2_b32 v[100:101], v234 offset0:24 offset1:25
	ds_read2_b32 v[102:103], v234 offset0:26 offset1:27
	s_waitcnt lgkmcnt(3)
	v_mul_f32_e32 v74, v74, v16
	v_mul_f32_e32 v58, v58, v16
	v_mul_f32_e32 v42, v42, v16
	v_mul_f32_e32 v26, v26, v16
	v_mul_f32_e32 v75, v75, v17
	v_mul_f32_e32 v59, v59, v17
	v_mul_f32_e32 v43, v43, v17
	v_mul_f32_e32 v27, v27, v17
	s_waitcnt lgkmcnt(2)
	v_mul_f32_e32 v76, v76, v98
	v_mul_f32_e32 v60, v60, v98
	v_mul_f32_e32 v44, v44, v98
	v_mul_f32_e32 v28, v28, v98
	v_mul_f32_e32 v77, v77, v99
	v_mul_f32_e32 v61, v61, v99
	v_mul_f32_e32 v45, v45, v99
	v_mul_f32_e32 v29, v29, v99
	s_waitcnt lgkmcnt(1)
	v_mul_f32_e32 v78, v78, v100
	v_mul_f32_e32 v62, v62, v100
	v_mul_f32_e32 v46, v46, v100
	v_mul_f32_e32 v30, v30, v100
	v_mul_f32_e32 v79, v79, v101
	v_mul_f32_e32 v63, v63, v101
	v_mul_f32_e32 v47, v47, v101
	v_mul_f32_e32 v31, v31, v101
	s_waitcnt lgkmcnt(0)
	v_mul_f32_e32 v80, v80, v102
	v_mul_f32_e32 v64, v64, v102
	v_mul_f32_e32 v48, v48, v102
	v_mul_f32_e32 v32, v32, v102
	v_mul_f32_e32 v81, v81, v103
	v_mul_f32_e32 v65, v65, v103
	v_mul_f32_e32 v49, v49, v103
	v_mul_f32_e32 v33, v33, v103
	s_nop 0
	s_nop 0
	s_nop 0
	s_nop 0
	s_nop 0
	s_nop 0
	s_nop 0
	s_nop 0
	s_nop 0
	s_nop 0
	s_nop 0
	s_nop 0
	s_nop 0

.LBB0_959:
	v_max_f32_e32 v16, v16, v16
	v_max_f32_e32 v17, 0, v16
	v_exp_f32_e64 v16, -v17
	v_cmp_gt_u32_e32 vcc, 32, v230
	s_and_saveexec_b64 s[2:3], vcc
	ds_write_b32 v235, v16
	s_or_b64 exec, exec, s[2:3]
	v_sub_f32_e32 v113, v113, v17
	v_sub_f32_e32 v112, v112, v17
	v_sub_f32_e32 v111, v111, v17
	v_sub_f32_e32 v110, v110, v17
	v_sub_f32_e32 v109, v109, v17
	v_sub_f32_e32 v108, v108, v17
	v_sub_f32_e32 v107, v107, v17
	v_sub_f32_e32 v106, v106, v17
	v_sub_f32_e32 v105, v105, v17
	v_sub_f32_e32 v104, v104, v17
	v_sub_f32_e32 v103, v103, v17
	v_sub_f32_e32 v102, v102, v17
	v_sub_f32_e32 v101, v101, v17
	v_sub_f32_e32 v100, v100, v17
	v_sub_f32_e32 v99, v99, v17
	v_sub_f32_e32 v98, v98, v17
	v_sub_f32_e32 v97, v97, v17
	v_sub_f32_e32 v96, v96, v17
	v_sub_f32_e32 v95, v95, v17
	v_sub_f32_e32 v94, v94, v17
	v_sub_f32_e32 v93, v93, v17
	v_sub_f32_e32 v92, v92, v17
	v_sub_f32_e32 v91, v91, v17
	v_sub_f32_e32 v90, v90, v17
	v_sub_f32_e32 v89, v89, v17
	v_sub_f32_e32 v88, v88, v17
	v_sub_f32_e32 v87, v87, v17
	v_sub_f32_e32 v86, v86, v17
	v_sub_f32_e32 v85, v85, v17
	v_sub_f32_e32 v84, v84, v17
	v_sub_f32_e32 v83, v83, v17
	v_sub_f32_e32 v82, v82, v17
	v_mul_f32_e32 v243, v243, v16
	s_branch .LBB0_953
	s_nop 0
	s_nop 0
	s_nop 0
	s_nop 0
	s_nop 0
	s_nop 0
	s_nop 0
	s_nop 0
.LBB0_962:
	v_mov_b32_e32 v52, v0
	s_barrier
	s_ashr_i32 s21, s20, 31
	v_readfirstlane_b32 s0, v52
	s_ashr_i32 s2, s0, 2
	s_and_b32 s29, s2, -16
	s_ashr_i32 s3, s0, 7
	v_lshlrev_b32_e32 v2, 4, v52
	v_and_b32_e32 v38, 48, v52
	v_mov_b32_e32 v39, 0
	v_and_b32_e32 v59, 48, v2
	v_lshl_add_u64 v[2:3], s[14:15], 0, v[38:39]
	s_mov_b64 s[0:1], 0x120000
	s_cmp_gt_i32 s3, -1
	v_lshl_add_u64 v[42:43], v[2:3], 0, s[0:1]
	s_cselect_b64 s[0:1], -1, 0
	s_cmp_gt_i32 s3, 0
	v_ashrrev_i32_e32 v58, 2, v52
	s_cselect_b64 s[16:17], -1, 0
	s_cmp_gt_i32 s3, 1
	s_movk_i32 s4, 0x1200
	v_and_b32_e32 v1, 63, v52
	s_cselect_b64 s[18:19], -1, 0
	s_cmp_gt_i32 s3, 2
	v_bfi_b32 v44, -16, s2, v52
	v_mad_i64_i32 v[2:3], s[2:3], v58, s4, 0
	v_mov_b32_e32 v8, 0x90000
	v_lshlrev_b32_e32 v1, 2, v1
	v_mad_i64_i32 v[2:3], s[2:3], s20, v8, v[2:3]
	v_xor_b32_e32 v45, 4, v1
	v_xor_b32_e32 v53, 8, v1
	s_cselect_b64 s[22:23], -1, 0
	v_and_b32_e32 v1, 3, v52
	s_add_u32 s2, s94, s46
	v_lshl_or_b32 v2, v1, 5, v2
	s_addc_u32 s3, s95, 0
	v_bfe_u32 v41, v52, 4, 2
	v_lshl_add_u64 v[46:47], s[2:3], 0, v[2:3]
	v_mad_i64_i32 v[2:3], s[4:5], v44, s4, 0
	v_lshlrev_b32_e32 v40, 3, v41
	v_mad_i64_i32 v[2:3], s[4:5], s20, v8, v[2:3]
	v_or_b32_e32 v2, v2, v40
	v_and_b32_e32 v55, 15, v52
	v_lshl_add_u64 v[2:3], s[2:3], 0, v[2:3]
	s_mov_b64 s[2:3], 0x10a00040
	v_lshl_add_u32 v4, v58, 1, 0
	v_add_u32_e32 v5, 0, v38
	v_mul_u32_u24_e32 v6, 0x110, v59
	v_mul_u32_u24_e32 v7, 0x110, v55
	v_lshl_add_u64 v[48:49], v[2:3], 0, s[2:3]
	v_cndmask_b32_e64 v2, 0, 1, s[0:1]
	s_mov_b64 s[24:25], 0
	s_mov_b64 s[26:27], 0x10a00200
	v_mov_b32_e32 v39, 0x3727c5ac
	s_mov_b32 s28, 0xf800000
	v_mov_b32_e32 v54, 0x260
	s_movk_i32 s30, 0x7fff
	v_add_u32_e32 v56, v4, v6
	v_cmp_ne_u32_e64 s[2:3], 1, v2
	v_add_u32_e32 v57, v5, v7
	v_mov_b32_e32 v60, 1
	v_readlane_b32 s51, v254, 39
	s_branch .LBB0_964
